# MLA loop: next-tile K/V staging LDS writes issued before the PV MFMAs instead of in the iteration tail
# speedup vs baseline: 1.0113x; 1.0017x over previous
; #define LAS __attribute__((address_space(3)))
; #define AT_MFMA(a, b, c) __builtin_amdgcn_mfma_f32_32x32x16_bf16((a), (b), (c), 0, 0, 0)
; template <bool MLA>
; __device__ __forceinline__ void attn_unit(const P& p, LAS unsigned char* lds, const int b, const int h, const int qb) {
;     ...
;             const LAS unsigned char* vb = kb + KT;
; #pragma unroll
;             for (int d0 = 0; d0 < 4; ++d0) { const LAS unsigned char* vr = vb + (32 * d0 + r32) * VSTR + hi * 16;
;                 o[d0] = AT_MFMA(pf0, *(const LAS bf16x8*)(vr), o[d0]); o[d0] = AT_MFMA(pf1, *(const LAS bf16x8*)(vr + 32), o[d0]);
;                 o[d0] = AT_MFMA(pf2, *(const LAS bf16x8*)(vr + 64), o[d0]); o[d0] = AT_MFMA(pf3, *(const LAS bf16x8*)(vr + 96), o[d0]); __builtin_amdgcn_sched_barrier(0); }
;         }
;         if (more) AT_WRITE(cb ^ 1);
.LBB0_715:
	ds_read_b128 v[108:111], v243 offset:30272
	ds_read_b128 v[220:223], v243 offset:30304
	v_cvt_pk_bf16_f32 v105, v14, v16
	v_cvt_pk_bf16_f32 v104, v10, v12
	v_cvt_pk_bf16_f32 v106, v84, v87
	v_cvt_pk_bf16_f32 v107, v98, v99
	v_cvt_pk_bf16_f32 v216, v83, v86
	v_cvt_pk_bf16_f32 v217, v88, v90
	v_cvt_pk_bf16_f32 v218, v92, v94
	v_cvt_pk_bf16_f32 v219, v101, v102
	v_cvt_pk_bf16_f32 v4, v4, v5
	v_cvt_pk_bf16_f32 v5, v6, v7
	v_cvt_pk_bf16_f32 v6, v8, v9
	v_cvt_pk_bf16_f32 v7, v11, v13
	v_cvt_pk_bf16_f32 v12, v15, v17
	v_cvt_pk_bf16_f32 v13, v82, v85
	v_cvt_pk_bf16_f32 v14, v89, v91
	v_cvt_pk_bf16_f32 v15, v93, v95
	s_andn2_b64 vcc, exec, s[86:87]
	s_cbranch_vccnz .Lmla_skipw0
	s_xor_b32 s0, s95, 1
	s_mul_i32 s0, s0, 0xac00
	s_add_i32 s0, s0, 0
	v_add_u32_e32 v8, s0, v199
	s_waitcnt vmcnt(4)
	ds_write_b128 v8, v[138:141]
	s_waitcnt vmcnt(3)
	ds_write_b128 v8, v[142:145] offset:12800
	v_add_u32_e32 v8, s0, v200
	s_waitcnt vmcnt(2)
	ds_write_b128 v8, v[170:173] offset:256
	v_add_u32_e32 v8, s0, v201
	v_add_u32_e32 v9, 0x6000, v8
	v_add_u32_e32 v8, 0x8800, v8
	s_waitcnt vmcnt(1)
	ds_write2_b64 v9, v[174:175], v[176:177] offset0:128 offset1:130
	s_waitcnt vmcnt(0)
	ds_write2_b64 v8, v[178:179], v[180:181] offset1:2
.Lmla_skipw0:
	s_waitcnt lgkmcnt(7)
	v_mfma_f32_32x32x16_bf16 v[66:81], v[104:107], v[228:231], v[66:81]
	ds_read_b128 v[228:231], v243 offset:34816
	s_waitcnt lgkmcnt(7)
	v_mfma_f32_32x32x16_bf16 v[66:81], v[216:219], v[232:235], v[66:81]
	ds_read_b128 v[232:235], v243 offset:34848
	s_waitcnt lgkmcnt(7)
	v_mfma_f32_32x32x16_bf16 v[66:81], v[4:7], v[236:239], v[66:81]
	ds_read_b128 v[236:239], v243 offset:34880
	s_waitcnt lgkmcnt(7)
	v_mfma_f32_32x32x16_bf16 v[66:81], v[12:15], v[244:247], v[66:81]
	ds_read_b128 v[244:247], v243 offset:34912
	s_waitcnt lgkmcnt(7)
	v_mfma_f32_32x32x16_bf16 v[50:65], v[104:107], v[248:251], v[50:65]
	ds_read_b128 v[248:251], v243 offset:39424
	s_waitcnt lgkmcnt(7)
	v_mfma_f32_32x32x16_bf16 v[50:65], v[216:219], v[252:255], v[50:65]
	ds_read_b128 v[252:255], v243 offset:39456
	s_waitcnt lgkmcnt(7)
	v_mfma_f32_32x32x16_bf16 v[50:65], v[4:7], v[108:111], v[50:65]
	ds_read_b128 v[108:111], v243 offset:39488
	s_waitcnt lgkmcnt(7)
	v_mfma_f32_32x32x16_bf16 v[50:65], v[12:15], v[220:223], v[50:65]
	ds_read_b128 v[220:223], v243 offset:39520
	s_waitcnt lgkmcnt(7)
	v_mfma_f32_32x32x16_bf16 v[34:49], v[104:107], v[228:231], v[34:49]
	s_waitcnt lgkmcnt(6)
	v_mfma_f32_32x32x16_bf16 v[34:49], v[216:219], v[232:235], v[34:49]
	s_waitcnt lgkmcnt(5)
	v_mfma_f32_32x32x16_bf16 v[34:49], v[4:7], v[236:239], v[34:49]
	s_waitcnt lgkmcnt(4)
	v_mfma_f32_32x32x16_bf16 v[34:49], v[12:15], v[244:247], v[34:49]
	s_waitcnt lgkmcnt(3)
	v_add_f32_e32 v17, v97, v100
	v_fmac_f32_e32 v17, v215, v96
	v_mfma_f32_32x32x16_bf16 v[18:33], v[104:107], v[248:251], v[18:33]
	s_waitcnt lgkmcnt(2)
	v_mfma_f32_32x32x16_bf16 v[18:33], v[216:219], v[252:255], v[18:33]
	s_waitcnt lgkmcnt(1)
	v_mfma_f32_32x32x16_bf16 v[18:33], v[4:7], v[108:111], v[18:33]
	s_waitcnt lgkmcnt(0)
	v_mfma_f32_32x32x16_bf16 v[18:33], v[12:15], v[220:223], v[18:33]
	v_mov_b32_e32 v215, v17
	s_branch .LBB0_718

; #define LAS __attribute__((address_space(3)))
; #define AT_MFMA(a, b, c) __builtin_amdgcn_mfma_f32_32x32x16_bf16((a), (b), (c), 0, 0, 0)
; template <bool MLA>
; __device__ __forceinline__ void attn_unit(const P& p, LAS unsigned char* lds, const int b, const int h, const int qb) {
;     ...
;             const LAS unsigned char* vb = kb + KT;
; #pragma unroll
;             for (int d0 = 0; d0 < 4; ++d0) { const LAS unsigned char* vr = vb + (32 * d0 + r32) * VSTR + hi * 16;
;                 o[d0] = AT_MFMA(pf0, *(const LAS bf16x8*)(vr), o[d0]); o[d0] = AT_MFMA(pf1, *(const LAS bf16x8*)(vr + 32), o[d0]);
;                 o[d0] = AT_MFMA(pf2, *(const LAS bf16x8*)(vr + 64), o[d0]); o[d0] = AT_MFMA(pf3, *(const LAS bf16x8*)(vr + 96), o[d0]); __builtin_amdgcn_sched_barrier(0); }
;         }
;         if (more) AT_WRITE(cb ^ 1);
.LBB0_881:
	ds_read_b128 v[108:111], v243 offset:30272
	ds_read_b128 v[224:227], v243 offset:30304
	v_cvt_pk_bf16_f32 v105, v14, v16
	v_cvt_pk_bf16_f32 v104, v10, v12
	v_cvt_pk_bf16_f32 v106, v84, v87
	v_cvt_pk_bf16_f32 v107, v98, v99
	v_cvt_pk_bf16_f32 v220, v83, v86
	v_cvt_pk_bf16_f32 v221, v88, v90
	v_cvt_pk_bf16_f32 v222, v92, v94
	v_cvt_pk_bf16_f32 v223, v101, v102
	v_cvt_pk_bf16_f32 v4, v4, v5
	v_cvt_pk_bf16_f32 v5, v6, v7
	v_cvt_pk_bf16_f32 v6, v8, v9
	v_cvt_pk_bf16_f32 v7, v11, v13
	v_cvt_pk_bf16_f32 v12, v15, v17
	v_cvt_pk_bf16_f32 v13, v82, v85
	v_cvt_pk_bf16_f32 v14, v89, v91
	v_cvt_pk_bf16_f32 v15, v93, v95
	s_andn2_b64 vcc, exec, s[86:87]
	s_cbranch_vccnz .Lmla_skipw1
	s_xor_b32 s0, s95, 1
	s_mul_i32 s0, s0, 0xac00
	s_add_i32 s0, s0, 0
	v_add_u32_e32 v8, s0, v202
	s_waitcnt vmcnt(4)
	ds_write_b128 v8, v[138:141]
	s_waitcnt vmcnt(3)
	ds_write_b128 v8, v[142:145] offset:12800
	v_add_u32_e32 v8, s0, v203
	s_waitcnt vmcnt(2)
	ds_write_b128 v8, v[170:173] offset:256
	v_add_u32_e32 v8, s0, v204
	v_add_u32_e32 v9, 0x6000, v8
	v_add_u32_e32 v8, 0x8800, v8
	s_waitcnt vmcnt(1)
	ds_write2_b64 v9, v[174:175], v[176:177] offset0:128 offset1:130
	s_waitcnt vmcnt(0)
	ds_write2_b64 v8, v[178:179], v[180:181] offset1:2
.Lmla_skipw1:
	s_waitcnt lgkmcnt(7)
	v_mfma_f32_32x32x16_bf16 v[66:81], v[104:107], v[228:231], v[66:81]
	ds_read_b128 v[228:231], v243 offset:34816
	s_waitcnt lgkmcnt(7)
	v_mfma_f32_32x32x16_bf16 v[66:81], v[220:223], v[232:235], v[66:81]
	ds_read_b128 v[232:235], v243 offset:34848
	s_waitcnt lgkmcnt(7)
	v_mfma_f32_32x32x16_bf16 v[66:81], v[4:7], v[236:239], v[66:81]
	ds_read_b128 v[236:239], v243 offset:34880
	s_waitcnt lgkmcnt(7)
	v_mfma_f32_32x32x16_bf16 v[66:81], v[12:15], v[244:247], v[66:81]
	ds_read_b128 v[244:247], v243 offset:34912
	s_waitcnt lgkmcnt(7)
	v_mfma_f32_32x32x16_bf16 v[50:65], v[104:107], v[248:251], v[50:65]
	ds_read_b128 v[248:251], v243 offset:39424
	s_waitcnt lgkmcnt(7)
	v_mfma_f32_32x32x16_bf16 v[50:65], v[220:223], v[252:255], v[50:65]
	ds_read_b128 v[252:255], v243 offset:39456
	s_waitcnt lgkmcnt(7)
	v_mfma_f32_32x32x16_bf16 v[50:65], v[4:7], v[108:111], v[50:65]
	ds_read_b128 v[108:111], v243 offset:39488
	s_waitcnt lgkmcnt(7)
	v_mfma_f32_32x32x16_bf16 v[50:65], v[12:15], v[224:227], v[50:65]
	ds_read_b128 v[224:227], v243 offset:39520
	s_waitcnt lgkmcnt(7)
	v_mfma_f32_32x32x16_bf16 v[34:49], v[104:107], v[228:231], v[34:49]
	s_waitcnt lgkmcnt(6)
	v_mfma_f32_32x32x16_bf16 v[34:49], v[220:223], v[232:235], v[34:49]
	s_waitcnt lgkmcnt(5)
	v_mfma_f32_32x32x16_bf16 v[34:49], v[4:7], v[236:239], v[34:49]
	s_waitcnt lgkmcnt(4)
	v_mfma_f32_32x32x16_bf16 v[34:49], v[12:15], v[244:247], v[34:49]
	s_waitcnt lgkmcnt(3)
	v_add_f32_e32 v17, v97, v100
	v_fmac_f32_e32 v17, v218, v96
	v_mfma_f32_32x32x16_bf16 v[18:33], v[104:107], v[248:251], v[18:33]
	s_waitcnt lgkmcnt(2)
	v_mfma_f32_32x32x16_bf16 v[18:33], v[220:223], v[252:255], v[18:33]
	s_waitcnt lgkmcnt(1)
	v_mfma_f32_32x32x16_bf16 v[18:33], v[4:7], v[108:111], v[18:33]
	s_waitcnt lgkmcnt(0)
	v_mfma_f32_32x32x16_bf16 v[18:33], v[12:15], v[224:227], v[18:33]
	v_mov_b32_e32 v218, v17
	s_branch .LBB0_884
